# speedup vs baseline: 1.0944x; 1.0085x over previous
.LBB1_13:
	v_add_u32_e32 v147, v149, v148
	ds_read_b128 v[180:183], v147
	ds_read_b128 v[184:187], v147 offset:1024
	ds_read_b128 v[188:191], v147 offset:256
	ds_read_b128 v[192:195], v147 offset:1280
	s_add_i32 s26, s22, s21
	v_add_u32_e32 v147, v162, v158
	v_add_u32_e32 v248, v162, v159
	v_add_u32_e32 v249, v162, v160
	v_add_u32_e32 v250, v162, v161
	ds_read_b128 v[196:199], v147
	ds_read_b128 v[200:203], v147 offset:1024
	ds_read_b128 v[204:207], v248
	ds_read_b128 v[208:211], v248 offset:1024
	ds_read_b128 v[212:215], v249
	ds_read_b128 v[216:219], v249 offset:1024
	ds_read_b128 v[220:223], v250
	ds_read_b128 v[224:227], v250 offset:1024
	s_waitcnt lgkmcnt(8)
	s_barrier
	s_waitcnt lgkmcnt(0)
	s_setprio 1
	s_waitcnt lgkmcnt(0)
	v_mfma_f32_16x16x32_f16 v[124:127], v[180:183], v[196:199], v[124:127]
	v_mfma_f32_16x16x32_f16 v[120:123], v[188:191], v[196:199], v[120:123]
	s_add_i32 s24, s26, 1
	s_ashr_i32 s25, s24, 31
	v_mfma_f32_16x16x32_f16 v[116:119], v[180:183], v[204:207], v[116:119]
	s_lshl_b64 s[24:25], s[24:25], 7
	v_add_u32_e32 v232, 0xc000, v163
	v_mfma_f32_16x16x32_f16 v[112:115], v[188:191], v[204:207], v[112:115]
	v_lshl_add_u64 v[228:229], v[138:139], 0, s[24:25]
	v_readfirstlane_b32 s24, v232
	v_mfma_f32_16x16x32_f16 v[108:111], v[180:183], v[212:215], v[108:111]
	v_add_u32_e32 v232, 0xe000, v163
	v_lshl_add_u64 v[230:231], v[228:229], 0, v[134:135]
	v_mfma_f32_16x16x32_f16 v[104:107], v[188:191], v[212:215], v[104:107]
	s_mov_b32 m0, s24
	v_readfirstlane_b32 s24, v232
	v_mfma_f32_16x16x32_f16 v[100:103], v[180:183], v[220:223], v[100:103]
	global_load_lds_dwordx4 v[230:231], off
	v_mfma_f32_16x16x32_f16 v[96:99], v[188:191], v[220:223], v[96:99]
	v_lshl_add_u64 v[228:229], v[228:229], 0, v[136:137]
	s_mov_b32 m0, s24
	v_mfma_f32_16x16x32_f16 v[124:127], v[184:187], v[200:203], v[124:127]
	global_load_lds_dwordx4 v[228:229], off
	v_mfma_f32_16x16x32_f16 v[120:123], v[192:195], v[200:203], v[120:123]
	v_mfma_f32_16x16x32_f16 v[116:119], v[184:187], v[208:211], v[116:119]
	v_mfma_f32_16x16x32_f16 v[112:115], v[192:195], v[208:211], v[112:115]
	v_mfma_f32_16x16x32_f16 v[108:111], v[184:187], v[216:219], v[108:111]
	v_mfma_f32_16x16x32_f16 v[104:107], v[192:195], v[216:219], v[104:107]
	v_mfma_f32_16x16x32_f16 v[100:103], v[184:187], v[224:227], v[100:103]
	v_mfma_f32_16x16x32_f16 v[96:99], v[192:195], v[224:227], v[96:99]
	s_setprio 0
	s_barrier
	s_add_i32 s24, s26, 2
	s_ashr_i32 s25, s24, 31
	s_lshl_b64 s[24:25], s[24:25], 7
	v_lshl_add_u64 v[244:245], v[140:141], 0, s[24:25]
	v_readfirstlane_b32 s27, v173
	v_add_u32_e32 v240, v150, v148
	v_lshl_add_u64 v[246:247], v[244:245], 0, v[134:135]
	s_mov_b32 m0, s27
	v_readfirstlane_b32 s27, v174
	ds_read_b128 v[228:231], v240
	ds_read_b128 v[232:235], v240 offset:1024
	ds_read_b128 v[236:239], v240 offset:256
	ds_read_b128 v[240:243], v240 offset:1280
	s_add_i32 s21, s21, 2
	s_barrier
	s_waitcnt lgkmcnt(0)
	s_setprio 1
	s_waitcnt lgkmcnt(0)
	v_mfma_f32_16x16x32_f16 v[92:95], v[228:231], v[196:199], v[92:95]
	v_mfma_f32_16x16x32_f16 v[88:91], v[236:239], v[196:199], v[88:91]
	global_load_lds_dwordx4 v[246:247], off
	v_mfma_f32_16x16x32_f16 v[84:87], v[228:231], v[204:207], v[84:87]
	v_lshl_add_u64 v[244:245], v[244:245], 0, v[136:137]
	s_mov_b32 m0, s27
	v_mfma_f32_16x16x32_f16 v[80:83], v[236:239], v[204:207], v[80:83]
	global_load_lds_dwordx4 v[244:245], off
	v_mfma_f32_16x16x32_f16 v[76:79], v[228:231], v[212:215], v[76:79]
	v_mfma_f32_16x16x32_f16 v[72:75], v[236:239], v[212:215], v[72:75]
	v_mfma_f32_16x16x32_f16 v[68:71], v[228:231], v[220:223], v[68:71]
	v_mfma_f32_16x16x32_f16 v[64:67], v[236:239], v[220:223], v[64:67]
	v_mfma_f32_16x16x32_f16 v[92:95], v[232:235], v[200:203], v[92:95]
	v_mfma_f32_16x16x32_f16 v[88:91], v[240:243], v[200:203], v[88:91]
	v_lshl_add_u64 v[244:245], v[142:143], 0, s[24:25]
	v_readfirstlane_b32 s27, v163
	v_mfma_f32_16x16x32_f16 v[84:87], v[232:235], v[208:211], v[84:87]
	v_lshl_add_u64 v[246:247], v[244:245], 0, v[134:135]
	s_mov_b32 m0, s27
	v_mfma_f32_16x16x32_f16 v[80:83], v[240:243], v[208:211], v[80:83]
	v_readfirstlane_b32 s27, v164
	v_mfma_f32_16x16x32_f16 v[76:79], v[232:235], v[216:219], v[76:79]
	v_mfma_f32_16x16x32_f16 v[72:75], v[240:243], v[216:219], v[72:75]
	v_mfma_f32_16x16x32_f16 v[68:71], v[232:235], v[224:227], v[68:71]
	v_mfma_f32_16x16x32_f16 v[64:67], v[240:243], v[224:227], v[64:67]
	s_setprio 0
	s_barrier
	ds_read_b128 v[196:199], v147 offset:16384
	ds_read_b128 v[200:203], v147 offset:17408
	ds_read_b128 v[204:207], v248 offset:16384
	ds_read_b128 v[208:211], v248 offset:17408
	ds_read_b128 v[212:215], v249 offset:16384
	ds_read_b128 v[216:219], v249 offset:17408
	ds_read_b128 v[220:223], v250 offset:16384
	ds_read_b128 v[224:227], v250 offset:17408
	s_barrier
	s_waitcnt lgkmcnt(0)
	s_setprio 1
	s_waitcnt lgkmcnt(0)
	v_mfma_f32_16x16x32_f16 v[60:63], v[180:183], v[196:199], v[60:63]
	v_mfma_f32_16x16x32_f16 v[56:59], v[188:191], v[196:199], v[56:59]
	v_mfma_f32_16x16x32_f16 v[52:55], v[180:183], v[204:207], v[52:55]
	v_mfma_f32_16x16x32_f16 v[48:51], v[188:191], v[204:207], v[48:51]
	v_mfma_f32_16x16x32_f16 v[44:47], v[180:183], v[212:215], v[44:47]
	v_mfma_f32_16x16x32_f16 v[40:43], v[188:191], v[212:215], v[40:43]
	v_mfma_f32_16x16x32_f16 v[36:39], v[180:183], v[220:223], v[36:39]
	v_mfma_f32_16x16x32_f16 v[32:35], v[188:191], v[220:223], v[32:35]
	v_mfma_f32_16x16x32_f16 v[60:63], v[184:187], v[200:203], v[60:63]
	v_mfma_f32_16x16x32_f16 v[56:59], v[192:195], v[200:203], v[56:59]
	v_mfma_f32_16x16x32_f16 v[52:55], v[184:187], v[208:211], v[52:55]
	v_mfma_f32_16x16x32_f16 v[48:51], v[192:195], v[208:211], v[48:51]
	v_mfma_f32_16x16x32_f16 v[44:47], v[184:187], v[216:219], v[44:47]
	v_mfma_f32_16x16x32_f16 v[40:43], v[192:195], v[216:219], v[40:43]
	v_mfma_f32_16x16x32_f16 v[36:39], v[184:187], v[224:227], v[36:39]
	v_mfma_f32_16x16x32_f16 v[32:35], v[192:195], v[224:227], v[32:35]
	s_setprio 0
	s_barrier
	global_load_lds_dwordx4 v[246:247], off
	v_lshl_add_u64 v[244:245], v[244:245], 0, v[136:137]
	s_mov_b32 m0, s27
	s_nop 0
	global_load_lds_dwordx4 v[244:245], off
	v_lshl_add_u64 v[180:181], v[144:145], 0, s[24:25]
	v_readfirstlane_b32 s27, v175
	v_lshl_add_u64 v[182:183], v[180:181], 0, v[134:135]
	s_mov_b32 m0, s27
	v_readfirstlane_b32 s27, v176
	global_load_lds_dwordx4 v[182:183], off
	v_lshl_add_u64 v[180:181], v[180:181], 0, v[136:137]
	s_mov_b32 m0, s27
	s_nop 0
	global_load_lds_dwordx4 v[180:181], off
	s_waitcnt vmcnt(6)
	s_barrier
	s_setprio 1
	v_mfma_f32_16x16x32_f16 v[28:31], v[228:231], v[196:199], v[28:31]
	v_mfma_f32_16x16x32_f16 v[24:27], v[236:239], v[196:199], v[24:27]
	v_mfma_f32_16x16x32_f16 v[20:23], v[228:231], v[204:207], v[20:23]
	v_mfma_f32_16x16x32_f16 v[16:19], v[236:239], v[204:207], v[16:19]
	v_mfma_f32_16x16x32_f16 v[12:15], v[228:231], v[212:215], v[12:15]
	v_mfma_f32_16x16x32_f16 v[8:11], v[236:239], v[212:215], v[8:11]
	v_mfma_f32_16x16x32_f16 v[4:7], v[228:231], v[220:223], v[4:7]
	v_mfma_f32_16x16x32_f16 v[0:3], v[236:239], v[220:223], v[0:3]
	v_mfma_f32_16x16x32_f16 v[28:31], v[232:235], v[200:203], v[28:31]
	v_mfma_f32_16x16x32_f16 v[24:27], v[240:243], v[200:203], v[24:27]
	v_mfma_f32_16x16x32_f16 v[20:23], v[232:235], v[208:211], v[20:23]
	v_mfma_f32_16x16x32_f16 v[16:19], v[240:243], v[208:211], v[16:19]
	v_mfma_f32_16x16x32_f16 v[12:15], v[232:235], v[216:219], v[12:15]
	v_mfma_f32_16x16x32_f16 v[8:11], v[240:243], v[216:219], v[8:11]
	v_mfma_f32_16x16x32_f16 v[4:7], v[232:235], v[224:227], v[4:7]
	v_mfma_f32_16x16x32_f16 v[0:3], v[240:243], v[224:227], v[0:3]
	s_setprio 0
	v_add_u32_e32 v192, v151, v148
	s_barrier
	ds_read_b128 v[180:183], v192
	ds_read_b128 v[184:187], v192 offset:1024
	ds_read_b128 v[188:191], v192 offset:256
	ds_read_b128 v[192:195], v192 offset:1280
	ds_read_b128 v[196:199], v147 offset:32768
	ds_read_b128 v[200:203], v147 offset:33792
	ds_read_b128 v[204:207], v248 offset:32768
	ds_read_b128 v[208:211], v248 offset:33792
	ds_read_b128 v[212:215], v249 offset:32768
	ds_read_b128 v[216:219], v249 offset:33792
	ds_read_b128 v[220:223], v250 offset:32768
	ds_read_b128 v[224:227], v250 offset:33792
	s_waitcnt lgkmcnt(8)
	s_barrier
	s_waitcnt lgkmcnt(0)
	s_setprio 1
	s_waitcnt lgkmcnt(0)
	v_mfma_f32_16x16x32_f16 v[124:127], v[180:183], v[196:199], v[124:127]
	v_mfma_f32_16x16x32_f16 v[120:123], v[188:191], v[196:199], v[120:123]
	v_mfma_f32_16x16x32_f16 v[116:119], v[180:183], v[204:207], v[116:119]
	v_lshl_add_u64 v[228:229], v[138:139], 0, s[24:25]
	v_readfirstlane_b32 s24, v165
	v_mfma_f32_16x16x32_f16 v[112:115], v[188:191], v[204:207], v[112:115]
	v_lshl_add_u64 v[230:231], v[228:229], 0, v[134:135]
	s_mov_b32 m0, s24
	v_mfma_f32_16x16x32_f16 v[108:111], v[180:183], v[212:215], v[108:111]
	v_readfirstlane_b32 s24, v166
	v_mfma_f32_16x16x32_f16 v[104:107], v[188:191], v[212:215], v[104:107]
	global_load_lds_dwordx4 v[230:231], off
	v_mfma_f32_16x16x32_f16 v[100:103], v[180:183], v[220:223], v[100:103]
	v_lshl_add_u64 v[228:229], v[228:229], 0, v[136:137]
	s_mov_b32 m0, s24
	v_mfma_f32_16x16x32_f16 v[96:99], v[188:191], v[220:223], v[96:99]
	global_load_lds_dwordx4 v[228:229], off
	v_mfma_f32_16x16x32_f16 v[124:127], v[184:187], v[200:203], v[124:127]
	v_mfma_f32_16x16x32_f16 v[120:123], v[192:195], v[200:203], v[120:123]
	v_mfma_f32_16x16x32_f16 v[116:119], v[184:187], v[208:211], v[116:119]
	v_mfma_f32_16x16x32_f16 v[112:115], v[192:195], v[208:211], v[112:115]
	v_mfma_f32_16x16x32_f16 v[108:111], v[184:187], v[216:219], v[108:111]
	v_mfma_f32_16x16x32_f16 v[104:107], v[192:195], v[216:219], v[104:107]
	v_mfma_f32_16x16x32_f16 v[100:103], v[184:187], v[224:227], v[100:103]
	v_mfma_f32_16x16x32_f16 v[96:99], v[192:195], v[224:227], v[96:99]
	s_setprio 0
	s_barrier
	s_add_i32 s24, s26, 3
	s_ashr_i32 s25, s24, 31
	s_lshl_b64 s[24:25], s[24:25], 7
	v_lshl_add_u64 v[244:245], v[140:141], 0, s[24:25]
	v_readfirstlane_b32 s26, v177
	v_add_u32_e32 v240, v152, v148
	v_lshl_add_u64 v[246:247], v[244:245], 0, v[134:135]
	s_mov_b32 m0, s26
	v_readfirstlane_b32 s26, v178
	ds_read_b128 v[228:231], v240
	ds_read_b128 v[232:235], v240 offset:1024
	ds_read_b128 v[236:239], v240 offset:256
	ds_read_b128 v[240:243], v240 offset:1280
	s_barrier
	s_waitcnt lgkmcnt(0)
	s_setprio 1
	s_waitcnt lgkmcnt(0)
	v_mfma_f32_16x16x32_f16 v[92:95], v[228:231], v[196:199], v[92:95]
	v_mfma_f32_16x16x32_f16 v[88:91], v[236:239], v[196:199], v[88:91]
	global_load_lds_dwordx4 v[246:247], off
	v_mfma_f32_16x16x32_f16 v[84:87], v[228:231], v[204:207], v[84:87]
	v_lshl_add_u64 v[244:245], v[244:245], 0, v[136:137]
	s_mov_b32 m0, s26
	v_mfma_f32_16x16x32_f16 v[80:83], v[236:239], v[204:207], v[80:83]
	global_load_lds_dwordx4 v[244:245], off
	v_mfma_f32_16x16x32_f16 v[76:79], v[228:231], v[212:215], v[76:79]
	v_mfma_f32_16x16x32_f16 v[72:75], v[236:239], v[212:215], v[72:75]
	v_mfma_f32_16x16x32_f16 v[68:71], v[228:231], v[220:223], v[68:71]
	v_mfma_f32_16x16x32_f16 v[64:67], v[236:239], v[220:223], v[64:67]
	v_mfma_f32_16x16x32_f16 v[92:95], v[232:235], v[200:203], v[92:95]
	v_mfma_f32_16x16x32_f16 v[88:91], v[240:243], v[200:203], v[88:91]
	v_lshl_add_u64 v[244:245], v[142:143], 0, s[24:25]
	v_readfirstlane_b32 s26, v167
	v_mfma_f32_16x16x32_f16 v[84:87], v[232:235], v[208:211], v[84:87]
	v_lshl_add_u64 v[246:247], v[244:245], 0, v[134:135]
	s_mov_b32 m0, s26
	v_mfma_f32_16x16x32_f16 v[80:83], v[240:243], v[208:211], v[80:83]
	v_readfirstlane_b32 s26, v168
	v_mfma_f32_16x16x32_f16 v[76:79], v[232:235], v[216:219], v[76:79]
	v_mfma_f32_16x16x32_f16 v[72:75], v[240:243], v[216:219], v[72:75]
	v_mfma_f32_16x16x32_f16 v[68:71], v[232:235], v[224:227], v[68:71]
	v_mfma_f32_16x16x32_f16 v[64:67], v[240:243], v[224:227], v[64:67]
	s_setprio 0
	s_barrier
	ds_read_b128 v[196:199], v147 offset:49152
	ds_read_b128 v[200:203], v147 offset:50176
	ds_read_b128 v[204:207], v248 offset:49152
	ds_read_b128 v[208:211], v248 offset:50176
	ds_read_b128 v[212:215], v249 offset:49152
	ds_read_b128 v[216:219], v249 offset:50176
	ds_read_b128 v[220:223], v250 offset:49152
	ds_read_b128 v[224:227], v250 offset:50176
	s_barrier
	s_waitcnt lgkmcnt(0)
	s_setprio 1
	s_waitcnt lgkmcnt(0)
	v_mfma_f32_16x16x32_f16 v[60:63], v[180:183], v[196:199], v[60:63]
	v_mfma_f32_16x16x32_f16 v[56:59], v[188:191], v[196:199], v[56:59]
	v_mfma_f32_16x16x32_f16 v[52:55], v[180:183], v[204:207], v[52:55]
	v_mfma_f32_16x16x32_f16 v[48:51], v[188:191], v[204:207], v[48:51]
	v_mfma_f32_16x16x32_f16 v[44:47], v[180:183], v[212:215], v[44:47]
	v_mfma_f32_16x16x32_f16 v[40:43], v[188:191], v[212:215], v[40:43]
	v_mfma_f32_16x16x32_f16 v[36:39], v[180:183], v[220:223], v[36:39]
	v_mfma_f32_16x16x32_f16 v[32:35], v[188:191], v[220:223], v[32:35]
	v_mfma_f32_16x16x32_f16 v[60:63], v[184:187], v[200:203], v[60:63]
	v_mfma_f32_16x16x32_f16 v[56:59], v[192:195], v[200:203], v[56:59]
	v_mfma_f32_16x16x32_f16 v[52:55], v[184:187], v[208:211], v[52:55]
	v_mfma_f32_16x16x32_f16 v[48:51], v[192:195], v[208:211], v[48:51]
	v_mfma_f32_16x16x32_f16 v[44:47], v[184:187], v[216:219], v[44:47]
	v_mfma_f32_16x16x32_f16 v[40:43], v[192:195], v[216:219], v[40:43]
	v_mfma_f32_16x16x32_f16 v[36:39], v[184:187], v[224:227], v[36:39]
	v_mfma_f32_16x16x32_f16 v[32:35], v[192:195], v[224:227], v[32:35]
	s_setprio 0
	s_barrier
	global_load_lds_dwordx4 v[246:247], off
	v_lshl_add_u64 v[244:245], v[244:245], 0, v[136:137]
	s_mov_b32 m0, s26
	s_nop 0
	global_load_lds_dwordx4 v[244:245], off
	v_lshl_add_u64 v[180:181], v[144:145], 0, s[24:25]
	v_readfirstlane_b32 s24, v179
	v_lshl_add_u64 v[182:183], v[180:181], 0, v[134:135]
	s_mov_b32 m0, s24
	v_readfirstlane_b32 s24, v146
	global_load_lds_dwordx4 v[182:183], off
	v_lshl_add_u64 v[180:181], v[180:181], 0, v[136:137]
	s_mov_b32 m0, s24
	s_nop 0
	global_load_lds_dwordx4 v[180:181], off
	s_waitcnt vmcnt(6)
	s_barrier
	s_setprio 1
	v_mfma_f32_16x16x32_f16 v[28:31], v[228:231], v[196:199], v[28:31]
	v_mfma_f32_16x16x32_f16 v[24:27], v[236:239], v[196:199], v[24:27]
	v_mfma_f32_16x16x32_f16 v[20:23], v[228:231], v[204:207], v[20:23]
	v_mfma_f32_16x16x32_f16 v[16:19], v[236:239], v[204:207], v[16:19]
	v_mfma_f32_16x16x32_f16 v[12:15], v[228:231], v[212:215], v[12:15]
	v_mfma_f32_16x16x32_f16 v[8:11], v[236:239], v[212:215], v[8:11]
	v_mfma_f32_16x16x32_f16 v[4:7], v[228:231], v[220:223], v[4:7]
	v_mfma_f32_16x16x32_f16 v[0:3], v[236:239], v[220:223], v[0:3]
	v_mfma_f32_16x16x32_f16 v[28:31], v[232:235], v[200:203], v[28:31]
	v_mfma_f32_16x16x32_f16 v[24:27], v[240:243], v[200:203], v[24:27]
	v_mfma_f32_16x16x32_f16 v[20:23], v[232:235], v[208:211], v[20:23]
	v_mfma_f32_16x16x32_f16 v[16:19], v[240:243], v[208:211], v[16:19]
	v_mfma_f32_16x16x32_f16 v[12:15], v[232:235], v[216:219], v[12:15]
	v_mfma_f32_16x16x32_f16 v[8:11], v[240:243], v[216:219], v[8:11]
	v_mfma_f32_16x16x32_f16 v[4:7], v[232:235], v[224:227], v[4:7]
	v_mfma_f32_16x16x32_f16 v[0:3], v[240:243], v[224:227], v[0:3]
	s_setprio 0
	s_cmp_ge_i32 s21, s5
	s_barrier
	s_cbranch_scc0 .LBB1_13

.Lrec_poll_chk:
	v_and_b32_e32 v52, 0x10001, v52
	v_cmp_eq_u32_e32 vcc, s4, v52
	s_andn2_b64 exec, exec, vcc
	s_cbranch_execnz .Lrec_retry

.Lrec_gate2:
	v_cndmask_b32_e64 v4, v2, v0, s[2:3]
	v_cndmask_b32_e64 v5, v1, v3, s[2:3]
	s_nop 0
	v_mov_b32_dpp v6, v4 row_ror:8 row_mask:0xf bank_mask:0xf
	v_mov_b32_dpp v7, v5 row_ror:8 row_mask:0xf bank_mask:0xf
	v_cndmask_b32_e64 v0, v0, v6, s[2:3]
	v_cndmask_b32_e64 v2, v6, v2, s[2:3]
	v_cndmask_b32_e64 v1, v7, v1, s[2:3]
	v_cndmask_b32_e64 v3, v3, v7, s[2:3]
	v_add_f32_e32 v2, v2, v112
	v_add_f32_e32 v0, v0, v113
	v_add_f32_e32 v1, v1, v114
	v_add_f32_e32 v3, v3, v115
	v_add_f32_e32 v0, v116, v0
	v_add_f32_e32 v3, v117, v3
	v_mul_f32_e32 v2, 0xbfb8aa3b, v2
	v_mul_f32_e32 v1, 0x4038aa3b, v1
	v_mul_f32_e32 v0, 0xbfb8aa3b, v0
	v_exp_f32_e32 v1, v1
	v_exp_f32_e32 v2, v2
	v_exp_f32_e32 v0, v0
	v_mul_f32_e32 v3, 0xbfb8aa3b, v3
	v_add_f32_e32 v1, 1.0, v1
	v_add_f32_e32 v2, 1.0, v2
	v_exp_f32_e32 v3, v3
	v_rcp_f32_e32 v1, v1
	v_add_f32_e32 v0, 1.0, v0
	v_rcp_f32_e32 v2, v2
	v_rcp_f32_e32 v5, v0
	v_add_f32_e32 v3, 1.0, v3
	v_fma_f32 v0, v1, -2.0, 1.0
	v_mul_f32_e32 v0, v2, v0
	v_rcp_f32_e32 v3, v3
	v_fmac_f32_e32 v0, v26, v5
	v_mul_f32_e32 v1, 0x4038aa3b, v0
	v_exp_f32_e32 v1, v1
	s_cmpk_eq_i32 s29, 0x7f
	v_add_f32_e32 v1, 1.0, v1
	v_rcp_f32_e32 v1, v1
	s_nop 0
	v_fma_f32 v1, v1, -2.0, 1.0
	v_mul_f32_e32 v46, v3, v1
	s_cbranch_scc1 .LBB2_29
	v_cvt_f16_f32_e32 v2, v46
	s_cmp_lg_u64 s[0:1], 0
	v_bitop3_b16 v2, s37, v2, -2 bitop3:0xf8
	s_cbranch_scc1 .Lrec_pub_slow
	global_store_short v120, v2, s[8:9]
	s_branch .LBB2_29

.LBB2_23:
	v_mov_b32_e32 v0, 0
	v_mov_b32_e32 v1, 0
	v_mov_b32_e32 v2, 0
	v_mov_b32_e32 v3, 0
	v_cvt_f32_f16_e32 v112, v44
	v_cvt_f32_f16_e32 v113, v43
	v_cvt_f32_f16_e32 v114, v42
	v_cvt_f32_f16_e32 v115, v41
	v_cvt_f32_f16_e32 v118, v45
	v_cndmask_b32_e64 v116, 0, v118, s[22:23]
	v_cndmask_b32_e64 v117, v118, 0, s[22:23]
	s_branch .Lrec_gate2
.Lrec_retry:
	s_add_i32 s31, s31, 1
	s_cmp_lg_u32 s6, 0
	s_cbranch_scc1 .Lrec_dead
	s_cmp_le_u32 s31, 0x10000
	s_cbranch_scc1 .Lrec_poll
.Lrec_dead:
	s_mov_b32 s6, 1
	s_branch .LBB2_20
